# speedup vs baseline: 1.0161x; 1.0161x over previous
.Lk_first:
	ds_read_b128 v[130:133], v219 offset:32768
	ds_read_b128 v[134:137], v219 offset:33792
	ds_read_b128 v[138:141], v219 offset:34816
	ds_read_b128 v[142:145], v219 offset:35840
	ds_read_b128 v[178:181], v219 offset:49152
	ds_read_b128 v[182:185], v219 offset:50176
	ds_read_b128 v[186:189], v219 offset:51200
	ds_read_b128 v[190:193], v219 offset:52224
	ds_read_b128 v[146:149], v220
	ds_read_b128 v[150:153], v220 offset:1024
	ds_read_b128 v[154:157], v221
	ds_read_b128 v[158:161], v221 offset:1024
	ds_read_b128 v[162:165], v222
	ds_read_b128 v[166:169], v222 offset:1024
	ds_read_b128 v[170:173], v223
	ds_read_b128 v[174:177], v223 offset:1024
	s_add_i32 s12, s8, 1
	s_mov_b32 m0, s43
	v_readlane_b32 s9, v248, s12
	s_nop 1
	v_add_u32_e32 v251, s9, v249
	global_load_lds_dwordx4 v251, s[18:19]
	v_add_u32_e32 v251, s9, v250
	s_mov_b32 m0, s44
	s_nop 0
	global_load_lds_dwordx4 v251, s[18:19]
	s_waitcnt lgkmcnt(0)
	s_barrier
	s_setprio 1
	v_mfma_f32_16x16x32_f16 v[124:127], v[130:133], v[146:149], 0
	v_mfma_f32_16x16x32_f16 v[124:127], v[134:137], v[150:153], v[124:127]
	v_mfma_f32_16x16x32_f16 v[120:123], v[138:141], v[146:149], 0
	v_mfma_f32_16x16x32_f16 v[120:123], v[142:145], v[150:153], v[120:123]
	v_mfma_f32_16x16x32_f16 v[116:119], v[130:133], v[154:157], 0
	v_mfma_f32_16x16x32_f16 v[116:119], v[134:137], v[158:161], v[116:119]
	v_mfma_f32_16x16x32_f16 v[112:115], v[138:141], v[154:157], 0
	v_mfma_f32_16x16x32_f16 v[112:115], v[142:145], v[158:161], v[112:115]
	v_mfma_f32_16x16x32_f16 v[108:111], v[130:133], v[162:165], 0
	v_mfma_f32_16x16x32_f16 v[108:111], v[134:137], v[166:169], v[108:111]
	v_mfma_f32_16x16x32_f16 v[104:107], v[138:141], v[162:165], 0
	v_mfma_f32_16x16x32_f16 v[104:107], v[142:145], v[166:169], v[104:107]
	v_mfma_f32_16x16x32_f16 v[100:103], v[130:133], v[170:173], 0
	v_mfma_f32_16x16x32_f16 v[100:103], v[134:137], v[174:177], v[100:103]
	v_mfma_f32_16x16x32_f16 v[96:99], v[138:141], v[170:173], 0
	v_mfma_f32_16x16x32_f16 v[96:99], v[142:145], v[174:177], v[96:99]
	v_mfma_f32_16x16x32_f16 v[52:55], v[178:181], v[146:149], 0
	v_mfma_f32_16x16x32_f16 v[52:55], v[182:185], v[150:153], v[52:55]
	v_mfma_f32_16x16x32_f16 v[40:43], v[186:189], v[146:149], 0
	v_mfma_f32_16x16x32_f16 v[40:43], v[190:193], v[150:153], v[40:43]
	v_mfma_f32_16x16x32_f16 v[36:39], v[178:181], v[154:157], 0
	v_mfma_f32_16x16x32_f16 v[36:39], v[182:185], v[158:161], v[36:39]
	v_mfma_f32_16x16x32_f16 v[32:35], v[186:189], v[154:157], 0
	v_mfma_f32_16x16x32_f16 v[32:35], v[190:193], v[158:161], v[32:35]
	v_mfma_f32_16x16x32_f16 v[28:31], v[178:181], v[162:165], 0
	v_mfma_f32_16x16x32_f16 v[28:31], v[182:185], v[166:169], v[28:31]
	v_mfma_f32_16x16x32_f16 v[24:27], v[186:189], v[162:165], 0
	v_mfma_f32_16x16x32_f16 v[24:27], v[190:193], v[166:169], v[24:27]
	v_mfma_f32_16x16x32_f16 v[20:23], v[178:181], v[170:173], 0
	v_mfma_f32_16x16x32_f16 v[20:23], v[182:185], v[174:177], v[20:23]
	v_mfma_f32_16x16x32_f16 v[16:19], v[186:189], v[170:173], 0
	v_mfma_f32_16x16x32_f16 v[16:19], v[190:193], v[174:177], v[16:19]
	s_setprio 0
	s_barrier
	ds_read_b128 v[146:149], v220 offset:16384
	ds_read_b128 v[150:153], v220 offset:17408
	ds_read_b128 v[154:157], v221 offset:16384
	ds_read_b128 v[158:161], v221 offset:17408
	ds_read_b128 v[162:165], v222 offset:16384
	ds_read_b128 v[166:169], v222 offset:17408
	ds_read_b128 v[170:173], v223 offset:16384
	ds_read_b128 v[174:177], v223 offset:17408
	v_add_u32_e32 v129, s7, v128
	s_mov_b32 m0, s22
	v_add_u32_e32 v194, 0xffffff80, v129
	global_load_lds_dwordx4 v194, s[10:11]
	v_add_u32_e32 v194, 0x47f80, v129
	s_mov_b32 m0, s23
	s_add_i32 s9, s8, 2
	global_load_lds_dwordx4 v194, s[10:11]
	v_readlane_b32 s13, v248, s9
	s_mov_b32 m0, s21
	s_nop 1
	v_add_u32_e32 v194, s13, v206
	global_load_lds_dwordx4 v194, s[18:19]
	v_add_u32_e32 v194, s13, v213
	s_mov_b32 m0, s24
	s_nop 0
	global_load_lds_dwordx4 v194, s[18:19]
	s_mov_b32 m0, s25
	v_add_u32_e32 v194, 0x8ff80, v129
	global_load_lds_dwordx4 v194, s[10:11]
	v_add_u32_e32 v194, 0xd7f80, v129
	s_mov_b32 m0, s26
	s_nop 0
	global_load_lds_dwordx4 v194, s[10:11]
	s_waitcnt vmcnt(8) lgkmcnt(0)
	s_barrier
	s_setprio 1
	v_mfma_f32_16x16x32_f16 v[12:15], v[130:133], v[146:149], 0
	v_mfma_f32_16x16x32_f16 v[12:15], v[134:137], v[150:153], v[12:15]
	v_mfma_f32_16x16x32_f16 v[8:11], v[138:141], v[146:149], 0
	v_mfma_f32_16x16x32_f16 v[8:11], v[142:145], v[150:153], v[8:11]
	v_mfma_f32_16x16x32_f16 v[4:7], v[130:133], v[154:157], 0
	v_mfma_f32_16x16x32_f16 v[4:7], v[134:137], v[158:161], v[4:7]
	v_mfma_f32_16x16x32_f16 v[0:3], v[138:141], v[154:157], 0
	v_mfma_f32_16x16x32_f16 v[0:3], v[142:145], v[158:161], v[0:3]
	v_mfma_f32_16x16x32_f16 v[44:47], v[130:133], v[162:165], 0
	v_mfma_f32_16x16x32_f16 v[44:47], v[134:137], v[166:169], v[44:47]
	v_mfma_f32_16x16x32_f16 v[48:51], v[138:141], v[162:165], 0
	v_mfma_f32_16x16x32_f16 v[48:51], v[142:145], v[166:169], v[48:51]
	v_mfma_f32_16x16x32_f16 v[56:59], v[130:133], v[170:173], 0
	v_mfma_f32_16x16x32_f16 v[56:59], v[134:137], v[174:177], v[56:59]
	v_mfma_f32_16x16x32_f16 v[60:63], v[138:141], v[170:173], 0
	v_mfma_f32_16x16x32_f16 v[60:63], v[142:145], v[174:177], v[60:63]
	v_mfma_f32_16x16x32_f16 v[64:67], v[178:181], v[146:149], 0
	v_mfma_f32_16x16x32_f16 v[64:67], v[182:185], v[150:153], v[64:67]
	v_mfma_f32_16x16x32_f16 v[68:71], v[186:189], v[146:149], 0
	v_mfma_f32_16x16x32_f16 v[68:71], v[190:193], v[150:153], v[68:71]
	v_mfma_f32_16x16x32_f16 v[72:75], v[178:181], v[154:157], 0
	v_mfma_f32_16x16x32_f16 v[72:75], v[182:185], v[158:161], v[72:75]
	v_mfma_f32_16x16x32_f16 v[76:79], v[186:189], v[154:157], 0
	v_mfma_f32_16x16x32_f16 v[76:79], v[190:193], v[158:161], v[76:79]
	v_mfma_f32_16x16x32_f16 v[80:83], v[178:181], v[162:165], 0
	v_mfma_f32_16x16x32_f16 v[80:83], v[182:185], v[166:169], v[80:83]
	v_mfma_f32_16x16x32_f16 v[84:87], v[186:189], v[162:165], 0
	v_mfma_f32_16x16x32_f16 v[84:87], v[190:193], v[166:169], v[84:87]
	v_mfma_f32_16x16x32_f16 v[88:91], v[178:181], v[170:173], 0
	v_mfma_f32_16x16x32_f16 v[88:91], v[182:185], v[174:177], v[88:91]
	v_mfma_f32_16x16x32_f16 v[92:95], v[186:189], v[170:173], 0
	v_mfma_f32_16x16x32_f16 v[92:95], v[190:193], v[174:177], v[92:95]
	s_setprio 0
	s_barrier
	ds_read_b128 v[130:133], v224
	ds_read_b128 v[134:137], v224 offset:1024
	ds_read_b128 v[138:141], v224 offset:2048
	ds_read_b128 v[142:145], v224 offset:3072
	ds_read_b128 v[178:181], v229
	ds_read_b128 v[182:185], v229 offset:1024
	ds_read_b128 v[186:189], v229 offset:2048
	ds_read_b128 v[190:193], v229 offset:3072
	ds_read_b128 v[146:149], v225
	ds_read_b128 v[150:153], v225 offset:1024
	ds_read_b128 v[154:157], v226
	ds_read_b128 v[158:161], v226 offset:1024
	ds_read_b128 v[162:165], v227
	ds_read_b128 v[166:169], v227 offset:1024
	ds_read_b128 v[170:173], v228
	ds_read_b128 v[174:177], v228 offset:1024
	v_readlane_b32 s12, v248, s9
	s_mov_b32 m0, s27
	s_nop 1
	v_add_u32_e32 v251, s12, v249
	global_load_lds_dwordx4 v251, s[18:19]
	v_add_u32_e32 v251, s12, v250
	s_mov_b32 m0, s28
	s_nop 0
	global_load_lds_dwordx4 v251, s[18:19]
	s_waitcnt vmcnt(8) lgkmcnt(0)
	s_barrier
	s_setprio 1
	v_mfma_f32_16x16x32_f16 v[124:127], v[130:133], v[146:149], v[124:127]
	v_mfma_f32_16x16x32_f16 v[124:127], v[134:137], v[150:153], v[124:127]
	v_mfma_f32_16x16x32_f16 v[120:123], v[138:141], v[146:149], v[120:123]
	v_mfma_f32_16x16x32_f16 v[120:123], v[142:145], v[150:153], v[120:123]
	v_mfma_f32_16x16x32_f16 v[116:119], v[130:133], v[154:157], v[116:119]
	v_mfma_f32_16x16x32_f16 v[116:119], v[134:137], v[158:161], v[116:119]
	v_mfma_f32_16x16x32_f16 v[112:115], v[138:141], v[154:157], v[112:115]
	v_mfma_f32_16x16x32_f16 v[112:115], v[142:145], v[158:161], v[112:115]
	v_mfma_f32_16x16x32_f16 v[108:111], v[130:133], v[162:165], v[108:111]
	v_mfma_f32_16x16x32_f16 v[108:111], v[134:137], v[166:169], v[108:111]
	v_mfma_f32_16x16x32_f16 v[104:107], v[138:141], v[162:165], v[104:107]
	v_mfma_f32_16x16x32_f16 v[104:107], v[142:145], v[166:169], v[104:107]
	v_mfma_f32_16x16x32_f16 v[100:103], v[130:133], v[170:173], v[100:103]
	v_mfma_f32_16x16x32_f16 v[100:103], v[134:137], v[174:177], v[100:103]
	v_mfma_f32_16x16x32_f16 v[96:99], v[138:141], v[170:173], v[96:99]
	v_mfma_f32_16x16x32_f16 v[96:99], v[142:145], v[174:177], v[96:99]
	v_mfma_f32_16x16x32_f16 v[52:55], v[178:181], v[146:149], v[52:55]
	v_mfma_f32_16x16x32_f16 v[52:55], v[182:185], v[150:153], v[52:55]
	v_mfma_f32_16x16x32_f16 v[40:43], v[186:189], v[146:149], v[40:43]
	v_mfma_f32_16x16x32_f16 v[40:43], v[190:193], v[150:153], v[40:43]
	v_mfma_f32_16x16x32_f16 v[36:39], v[178:181], v[154:157], v[36:39]
	v_mfma_f32_16x16x32_f16 v[36:39], v[182:185], v[158:161], v[36:39]
	v_mfma_f32_16x16x32_f16 v[32:35], v[186:189], v[154:157], v[32:35]
	v_mfma_f32_16x16x32_f16 v[32:35], v[190:193], v[158:161], v[32:35]
	v_mfma_f32_16x16x32_f16 v[28:31], v[178:181], v[162:165], v[28:31]
	v_mfma_f32_16x16x32_f16 v[28:31], v[182:185], v[166:169], v[28:31]
	v_mfma_f32_16x16x32_f16 v[24:27], v[186:189], v[162:165], v[24:27]
	v_mfma_f32_16x16x32_f16 v[24:27], v[190:193], v[166:169], v[24:27]
	v_mfma_f32_16x16x32_f16 v[20:23], v[178:181], v[170:173], v[20:23]
	v_mfma_f32_16x16x32_f16 v[20:23], v[182:185], v[174:177], v[20:23]
	v_mfma_f32_16x16x32_f16 v[16:19], v[186:189], v[170:173], v[16:19]
	v_mfma_f32_16x16x32_f16 v[16:19], v[190:193], v[174:177], v[16:19]
	s_setprio 0
	s_barrier
	ds_read_b128 v[146:149], v230
	ds_read_b128 v[150:153], v230 offset:1024
	ds_read_b128 v[154:157], v231
	ds_read_b128 v[158:161], v231 offset:1024
	ds_read_b128 v[162:165], v232
	ds_read_b128 v[166:169], v232 offset:1024
	ds_read_b128 v[170:173], v233
	ds_read_b128 v[174:177], v233 offset:1024
	s_mov_b32 m0, s37
	v_add_u32_e32 v194, 0x48000, v129
	global_load_lds_dwordx4 v129, s[10:11]
	s_mov_b32 m0, s38
	s_add_i32 s12, s8, 3
	global_load_lds_dwordx4 v194, s[10:11]
	v_readlane_b32 s13, v248, s12
	s_mov_b32 m0, s39
	s_nop 1
	v_add_u32_e32 v194, s13, v206
	global_load_lds_dwordx4 v194, s[18:19]
	v_add_u32_e32 v194, s13, v213
	s_mov_b32 m0, s40
	s_nop 0
	global_load_lds_dwordx4 v194, s[18:19]
	s_mov_b32 m0, s41
	v_add_u32_e32 v194, 0x90000, v129
	global_load_lds_dwordx4 v194, s[10:11]
	v_add_u32_e32 v194, 0xd8000, v129
	s_mov_b32 m0, s42
	s_nop 0
	global_load_lds_dwordx4 v194, s[10:11]
	s_waitcnt vmcnt(8) lgkmcnt(0)
	s_barrier
	s_setprio 1
	v_mfma_f32_16x16x32_f16 v[12:15], v[130:133], v[146:149], v[12:15]
	v_mfma_f32_16x16x32_f16 v[12:15], v[134:137], v[150:153], v[12:15]
	v_mfma_f32_16x16x32_f16 v[8:11], v[138:141], v[146:149], v[8:11]
	v_mfma_f32_16x16x32_f16 v[8:11], v[142:145], v[150:153], v[8:11]
	v_mfma_f32_16x16x32_f16 v[4:7], v[130:133], v[154:157], v[4:7]
	v_mfma_f32_16x16x32_f16 v[4:7], v[134:137], v[158:161], v[4:7]
	v_mfma_f32_16x16x32_f16 v[0:3], v[138:141], v[154:157], v[0:3]
	v_mfma_f32_16x16x32_f16 v[0:3], v[142:145], v[158:161], v[0:3]
	v_mfma_f32_16x16x32_f16 v[44:47], v[130:133], v[162:165], v[44:47]
	v_mfma_f32_16x16x32_f16 v[44:47], v[134:137], v[166:169], v[44:47]
	v_mfma_f32_16x16x32_f16 v[48:51], v[138:141], v[162:165], v[48:51]
	v_mfma_f32_16x16x32_f16 v[48:51], v[142:145], v[166:169], v[48:51]
	v_mfma_f32_16x16x32_f16 v[56:59], v[130:133], v[170:173], v[56:59]
	v_mfma_f32_16x16x32_f16 v[56:59], v[134:137], v[174:177], v[56:59]
	v_mfma_f32_16x16x32_f16 v[60:63], v[138:141], v[170:173], v[60:63]
	v_mfma_f32_16x16x32_f16 v[60:63], v[142:145], v[174:177], v[60:63]
	v_mfma_f32_16x16x32_f16 v[64:67], v[178:181], v[146:149], v[64:67]
	v_mfma_f32_16x16x32_f16 v[64:67], v[182:185], v[150:153], v[64:67]
	v_mfma_f32_16x16x32_f16 v[68:71], v[186:189], v[146:149], v[68:71]
	v_mfma_f32_16x16x32_f16 v[68:71], v[190:193], v[150:153], v[68:71]
	v_mfma_f32_16x16x32_f16 v[72:75], v[178:181], v[154:157], v[72:75]
	v_mfma_f32_16x16x32_f16 v[72:75], v[182:185], v[158:161], v[72:75]
	v_mfma_f32_16x16x32_f16 v[76:79], v[186:189], v[154:157], v[76:79]
	v_mfma_f32_16x16x32_f16 v[76:79], v[190:193], v[158:161], v[76:79]
	v_mfma_f32_16x16x32_f16 v[80:83], v[178:181], v[162:165], v[80:83]
	v_mfma_f32_16x16x32_f16 v[80:83], v[182:185], v[166:169], v[80:83]
	v_mfma_f32_16x16x32_f16 v[84:87], v[186:189], v[162:165], v[84:87]
	v_mfma_f32_16x16x32_f16 v[84:87], v[190:193], v[166:169], v[84:87]
	v_mfma_f32_16x16x32_f16 v[88:91], v[178:181], v[170:173], v[88:91]
	v_mfma_f32_16x16x32_f16 v[88:91], v[182:185], v[174:177], v[88:91]
	v_mfma_f32_16x16x32_f16 v[92:95], v[186:189], v[170:173], v[92:95]
	v_mfma_f32_16x16x32_f16 v[92:95], v[190:193], v[174:177], v[92:95]
	s_setprio 0
	s_addk_i32 s7, 0x100
	s_cmp_lt_u32 s8, 32
	s_mov_b32 s8, s9
	s_barrier
.LBB1_82:
	ds_read_b128 v[130:133], v219 offset:32768
	ds_read_b128 v[134:137], v219 offset:33792
	ds_read_b128 v[138:141], v219 offset:34816
	ds_read_b128 v[142:145], v219 offset:35840
	ds_read_b128 v[178:181], v219 offset:49152
	ds_read_b128 v[182:185], v219 offset:50176
	ds_read_b128 v[186:189], v219 offset:51200
	ds_read_b128 v[190:193], v219 offset:52224
	ds_read_b128 v[146:149], v220
	ds_read_b128 v[150:153], v220 offset:1024
	ds_read_b128 v[154:157], v221
	ds_read_b128 v[158:161], v221 offset:1024
	ds_read_b128 v[162:165], v222
	ds_read_b128 v[166:169], v222 offset:1024
	ds_read_b128 v[170:173], v223
	ds_read_b128 v[174:177], v223 offset:1024
	s_add_i32 s12, s8, 1
	s_mov_b32 m0, s43
	v_readlane_b32 s9, v248, s12
	s_nop 1
	v_add_u32_e32 v251, s9, v249
	global_load_lds_dwordx4 v251, s[18:19]
	v_add_u32_e32 v251, s9, v250
	s_mov_b32 m0, s44
	s_nop 0
	global_load_lds_dwordx4 v251, s[18:19]
	s_waitcnt vmcnt(8) lgkmcnt(0)
	s_barrier
	s_setprio 1
	v_mfma_f32_16x16x32_f16 v[124:127], v[130:133], v[146:149], v[124:127]
	v_mfma_f32_16x16x32_f16 v[124:127], v[134:137], v[150:153], v[124:127]
	v_mfma_f32_16x16x32_f16 v[120:123], v[138:141], v[146:149], v[120:123]
	v_mfma_f32_16x16x32_f16 v[120:123], v[142:145], v[150:153], v[120:123]
	v_mfma_f32_16x16x32_f16 v[116:119], v[130:133], v[154:157], v[116:119]
	v_mfma_f32_16x16x32_f16 v[116:119], v[134:137], v[158:161], v[116:119]
	v_mfma_f32_16x16x32_f16 v[112:115], v[138:141], v[154:157], v[112:115]
	v_mfma_f32_16x16x32_f16 v[112:115], v[142:145], v[158:161], v[112:115]
	v_mfma_f32_16x16x32_f16 v[108:111], v[130:133], v[162:165], v[108:111]
	v_mfma_f32_16x16x32_f16 v[108:111], v[134:137], v[166:169], v[108:111]
	v_mfma_f32_16x16x32_f16 v[104:107], v[138:141], v[162:165], v[104:107]
	v_mfma_f32_16x16x32_f16 v[104:107], v[142:145], v[166:169], v[104:107]
	v_mfma_f32_16x16x32_f16 v[100:103], v[130:133], v[170:173], v[100:103]
	v_mfma_f32_16x16x32_f16 v[100:103], v[134:137], v[174:177], v[100:103]
	v_mfma_f32_16x16x32_f16 v[96:99], v[138:141], v[170:173], v[96:99]
	v_mfma_f32_16x16x32_f16 v[96:99], v[142:145], v[174:177], v[96:99]
	v_mfma_f32_16x16x32_f16 v[52:55], v[178:181], v[146:149], v[52:55]
	v_mfma_f32_16x16x32_f16 v[52:55], v[182:185], v[150:153], v[52:55]
	v_mfma_f32_16x16x32_f16 v[40:43], v[186:189], v[146:149], v[40:43]
	v_mfma_f32_16x16x32_f16 v[40:43], v[190:193], v[150:153], v[40:43]
	v_mfma_f32_16x16x32_f16 v[36:39], v[178:181], v[154:157], v[36:39]
	v_mfma_f32_16x16x32_f16 v[36:39], v[182:185], v[158:161], v[36:39]
	v_mfma_f32_16x16x32_f16 v[32:35], v[186:189], v[154:157], v[32:35]
	v_mfma_f32_16x16x32_f16 v[32:35], v[190:193], v[158:161], v[32:35]
	v_mfma_f32_16x16x32_f16 v[28:31], v[178:181], v[162:165], v[28:31]
	v_mfma_f32_16x16x32_f16 v[28:31], v[182:185], v[166:169], v[28:31]
	v_mfma_f32_16x16x32_f16 v[24:27], v[186:189], v[162:165], v[24:27]
	v_mfma_f32_16x16x32_f16 v[24:27], v[190:193], v[166:169], v[24:27]
	v_mfma_f32_16x16x32_f16 v[20:23], v[178:181], v[170:173], v[20:23]
	v_mfma_f32_16x16x32_f16 v[20:23], v[182:185], v[174:177], v[20:23]
	v_mfma_f32_16x16x32_f16 v[16:19], v[186:189], v[170:173], v[16:19]
	v_mfma_f32_16x16x32_f16 v[16:19], v[190:193], v[174:177], v[16:19]
	s_setprio 0
	s_barrier
	ds_read_b128 v[146:149], v220 offset:16384
	ds_read_b128 v[150:153], v220 offset:17408
	ds_read_b128 v[154:157], v221 offset:16384
	ds_read_b128 v[158:161], v221 offset:17408
	ds_read_b128 v[162:165], v222 offset:16384
	ds_read_b128 v[166:169], v222 offset:17408
	ds_read_b128 v[170:173], v223 offset:16384
	ds_read_b128 v[174:177], v223 offset:17408
	v_add_u32_e32 v129, s7, v128
	s_mov_b32 m0, s22
	v_add_u32_e32 v194, 0xffffff80, v129
	global_load_lds_dwordx4 v194, s[10:11]
	v_add_u32_e32 v194, 0x47f80, v129
	s_mov_b32 m0, s23
	s_add_i32 s9, s8, 2
	global_load_lds_dwordx4 v194, s[10:11]
	v_readlane_b32 s13, v248, s9
	s_mov_b32 m0, s21
	s_nop 1
	v_add_u32_e32 v194, s13, v206
	global_load_lds_dwordx4 v194, s[18:19]
	v_add_u32_e32 v194, s13, v213
	s_mov_b32 m0, s24
	s_nop 0
	global_load_lds_dwordx4 v194, s[18:19]
	s_mov_b32 m0, s25
	v_add_u32_e32 v194, 0x8ff80, v129
	global_load_lds_dwordx4 v194, s[10:11]
	v_add_u32_e32 v194, 0xd7f80, v129
	s_mov_b32 m0, s26
	s_nop 0
	global_load_lds_dwordx4 v194, s[10:11]
	s_waitcnt vmcnt(8) lgkmcnt(0)
	s_barrier
	s_setprio 1
	v_mfma_f32_16x16x32_f16 v[12:15], v[130:133], v[146:149], v[12:15]
	v_mfma_f32_16x16x32_f16 v[12:15], v[134:137], v[150:153], v[12:15]
	v_mfma_f32_16x16x32_f16 v[8:11], v[138:141], v[146:149], v[8:11]
	v_mfma_f32_16x16x32_f16 v[8:11], v[142:145], v[150:153], v[8:11]
	v_mfma_f32_16x16x32_f16 v[4:7], v[130:133], v[154:157], v[4:7]
	v_mfma_f32_16x16x32_f16 v[4:7], v[134:137], v[158:161], v[4:7]
	v_mfma_f32_16x16x32_f16 v[0:3], v[138:141], v[154:157], v[0:3]
	v_mfma_f32_16x16x32_f16 v[0:3], v[142:145], v[158:161], v[0:3]
	v_mfma_f32_16x16x32_f16 v[44:47], v[130:133], v[162:165], v[44:47]
	v_mfma_f32_16x16x32_f16 v[44:47], v[134:137], v[166:169], v[44:47]
	v_mfma_f32_16x16x32_f16 v[48:51], v[138:141], v[162:165], v[48:51]
	v_mfma_f32_16x16x32_f16 v[48:51], v[142:145], v[166:169], v[48:51]
	v_mfma_f32_16x16x32_f16 v[56:59], v[130:133], v[170:173], v[56:59]
	v_mfma_f32_16x16x32_f16 v[56:59], v[134:137], v[174:177], v[56:59]
	v_mfma_f32_16x16x32_f16 v[60:63], v[138:141], v[170:173], v[60:63]
	v_mfma_f32_16x16x32_f16 v[60:63], v[142:145], v[174:177], v[60:63]
	v_mfma_f32_16x16x32_f16 v[64:67], v[178:181], v[146:149], v[64:67]
	v_mfma_f32_16x16x32_f16 v[64:67], v[182:185], v[150:153], v[64:67]
	v_mfma_f32_16x16x32_f16 v[68:71], v[186:189], v[146:149], v[68:71]
	v_mfma_f32_16x16x32_f16 v[68:71], v[190:193], v[150:153], v[68:71]
	v_mfma_f32_16x16x32_f16 v[72:75], v[178:181], v[154:157], v[72:75]
	v_mfma_f32_16x16x32_f16 v[72:75], v[182:185], v[158:161], v[72:75]
	v_mfma_f32_16x16x32_f16 v[76:79], v[186:189], v[154:157], v[76:79]
	v_mfma_f32_16x16x32_f16 v[76:79], v[190:193], v[158:161], v[76:79]
	v_mfma_f32_16x16x32_f16 v[80:83], v[178:181], v[162:165], v[80:83]
	v_mfma_f32_16x16x32_f16 v[80:83], v[182:185], v[166:169], v[80:83]
	v_mfma_f32_16x16x32_f16 v[84:87], v[186:189], v[162:165], v[84:87]
	v_mfma_f32_16x16x32_f16 v[84:87], v[190:193], v[166:169], v[84:87]
	v_mfma_f32_16x16x32_f16 v[88:91], v[178:181], v[170:173], v[88:91]
	v_mfma_f32_16x16x32_f16 v[88:91], v[182:185], v[174:177], v[88:91]
	v_mfma_f32_16x16x32_f16 v[92:95], v[186:189], v[170:173], v[92:95]
	v_mfma_f32_16x16x32_f16 v[92:95], v[190:193], v[174:177], v[92:95]
	s_setprio 0
	s_barrier
	ds_read_b128 v[130:133], v224
	ds_read_b128 v[134:137], v224 offset:1024
	ds_read_b128 v[138:141], v224 offset:2048
	ds_read_b128 v[142:145], v224 offset:3072
	ds_read_b128 v[178:181], v229
	ds_read_b128 v[182:185], v229 offset:1024
	ds_read_b128 v[186:189], v229 offset:2048
	ds_read_b128 v[190:193], v229 offset:3072
	ds_read_b128 v[146:149], v225
	ds_read_b128 v[150:153], v225 offset:1024
	ds_read_b128 v[154:157], v226
	ds_read_b128 v[158:161], v226 offset:1024
	ds_read_b128 v[162:165], v227
	ds_read_b128 v[166:169], v227 offset:1024
	ds_read_b128 v[170:173], v228
	ds_read_b128 v[174:177], v228 offset:1024
	v_readlane_b32 s12, v248, s9
	s_mov_b32 m0, s27
	s_nop 1
	v_add_u32_e32 v251, s12, v249
	global_load_lds_dwordx4 v251, s[18:19]
	v_add_u32_e32 v251, s12, v250
	s_mov_b32 m0, s28
	s_nop 0
	global_load_lds_dwordx4 v251, s[18:19]
	s_waitcnt vmcnt(8) lgkmcnt(0)
	s_barrier
	s_setprio 1
	v_mfma_f32_16x16x32_f16 v[124:127], v[130:133], v[146:149], v[124:127]
	v_mfma_f32_16x16x32_f16 v[124:127], v[134:137], v[150:153], v[124:127]
	v_mfma_f32_16x16x32_f16 v[120:123], v[138:141], v[146:149], v[120:123]
	v_mfma_f32_16x16x32_f16 v[120:123], v[142:145], v[150:153], v[120:123]
	v_mfma_f32_16x16x32_f16 v[116:119], v[130:133], v[154:157], v[116:119]
	v_mfma_f32_16x16x32_f16 v[116:119], v[134:137], v[158:161], v[116:119]
	v_mfma_f32_16x16x32_f16 v[112:115], v[138:141], v[154:157], v[112:115]
	v_mfma_f32_16x16x32_f16 v[112:115], v[142:145], v[158:161], v[112:115]
	v_mfma_f32_16x16x32_f16 v[108:111], v[130:133], v[162:165], v[108:111]
	v_mfma_f32_16x16x32_f16 v[108:111], v[134:137], v[166:169], v[108:111]
	v_mfma_f32_16x16x32_f16 v[104:107], v[138:141], v[162:165], v[104:107]
	v_mfma_f32_16x16x32_f16 v[104:107], v[142:145], v[166:169], v[104:107]
	v_mfma_f32_16x16x32_f16 v[100:103], v[130:133], v[170:173], v[100:103]
	v_mfma_f32_16x16x32_f16 v[100:103], v[134:137], v[174:177], v[100:103]
	v_mfma_f32_16x16x32_f16 v[96:99], v[138:141], v[170:173], v[96:99]
	v_mfma_f32_16x16x32_f16 v[96:99], v[142:145], v[174:177], v[96:99]
	v_mfma_f32_16x16x32_f16 v[52:55], v[178:181], v[146:149], v[52:55]
	v_mfma_f32_16x16x32_f16 v[52:55], v[182:185], v[150:153], v[52:55]
	v_mfma_f32_16x16x32_f16 v[40:43], v[186:189], v[146:149], v[40:43]
	v_mfma_f32_16x16x32_f16 v[40:43], v[190:193], v[150:153], v[40:43]
	v_mfma_f32_16x16x32_f16 v[36:39], v[178:181], v[154:157], v[36:39]
	v_mfma_f32_16x16x32_f16 v[36:39], v[182:185], v[158:161], v[36:39]
	v_mfma_f32_16x16x32_f16 v[32:35], v[186:189], v[154:157], v[32:35]
	v_mfma_f32_16x16x32_f16 v[32:35], v[190:193], v[158:161], v[32:35]
	v_mfma_f32_16x16x32_f16 v[28:31], v[178:181], v[162:165], v[28:31]
	v_mfma_f32_16x16x32_f16 v[28:31], v[182:185], v[166:169], v[28:31]
	v_mfma_f32_16x16x32_f16 v[24:27], v[186:189], v[162:165], v[24:27]
	v_mfma_f32_16x16x32_f16 v[24:27], v[190:193], v[166:169], v[24:27]
	v_mfma_f32_16x16x32_f16 v[20:23], v[178:181], v[170:173], v[20:23]
	v_mfma_f32_16x16x32_f16 v[20:23], v[182:185], v[174:177], v[20:23]
	v_mfma_f32_16x16x32_f16 v[16:19], v[186:189], v[170:173], v[16:19]
	v_mfma_f32_16x16x32_f16 v[16:19], v[190:193], v[174:177], v[16:19]
	s_setprio 0
	s_barrier
	ds_read_b128 v[146:149], v230
	ds_read_b128 v[150:153], v230 offset:1024
	ds_read_b128 v[154:157], v231
	ds_read_b128 v[158:161], v231 offset:1024
	ds_read_b128 v[162:165], v232
	ds_read_b128 v[166:169], v232 offset:1024
	ds_read_b128 v[170:173], v233
	ds_read_b128 v[174:177], v233 offset:1024
	s_mov_b32 m0, s37
	v_add_u32_e32 v194, 0x48000, v129
	global_load_lds_dwordx4 v129, s[10:11]
	s_mov_b32 m0, s38
	s_add_i32 s12, s8, 3
	global_load_lds_dwordx4 v194, s[10:11]
	v_readlane_b32 s13, v248, s12
	s_mov_b32 m0, s39
	s_nop 1
	v_add_u32_e32 v194, s13, v206
	global_load_lds_dwordx4 v194, s[18:19]
	v_add_u32_e32 v194, s13, v213
	s_mov_b32 m0, s40
	s_nop 0
	global_load_lds_dwordx4 v194, s[18:19]
	s_mov_b32 m0, s41
	v_add_u32_e32 v194, 0x90000, v129
	global_load_lds_dwordx4 v194, s[10:11]
	v_add_u32_e32 v194, 0xd8000, v129
	s_mov_b32 m0, s42
	s_nop 0
	global_load_lds_dwordx4 v194, s[10:11]
	s_waitcnt vmcnt(8) lgkmcnt(0)
	s_barrier
	s_setprio 1
	v_mfma_f32_16x16x32_f16 v[12:15], v[130:133], v[146:149], v[12:15]
	v_mfma_f32_16x16x32_f16 v[12:15], v[134:137], v[150:153], v[12:15]
	v_mfma_f32_16x16x32_f16 v[8:11], v[138:141], v[146:149], v[8:11]
	v_mfma_f32_16x16x32_f16 v[8:11], v[142:145], v[150:153], v[8:11]
	v_mfma_f32_16x16x32_f16 v[4:7], v[130:133], v[154:157], v[4:7]
	v_mfma_f32_16x16x32_f16 v[4:7], v[134:137], v[158:161], v[4:7]
	v_mfma_f32_16x16x32_f16 v[0:3], v[138:141], v[154:157], v[0:3]
	v_mfma_f32_16x16x32_f16 v[0:3], v[142:145], v[158:161], v[0:3]
	v_mfma_f32_16x16x32_f16 v[44:47], v[130:133], v[162:165], v[44:47]
	v_mfma_f32_16x16x32_f16 v[44:47], v[134:137], v[166:169], v[44:47]
	v_mfma_f32_16x16x32_f16 v[48:51], v[138:141], v[162:165], v[48:51]
	v_mfma_f32_16x16x32_f16 v[48:51], v[142:145], v[166:169], v[48:51]
	v_mfma_f32_16x16x32_f16 v[56:59], v[130:133], v[170:173], v[56:59]
	v_mfma_f32_16x16x32_f16 v[56:59], v[134:137], v[174:177], v[56:59]
	v_mfma_f32_16x16x32_f16 v[60:63], v[138:141], v[170:173], v[60:63]
	v_mfma_f32_16x16x32_f16 v[60:63], v[142:145], v[174:177], v[60:63]
	v_mfma_f32_16x16x32_f16 v[64:67], v[178:181], v[146:149], v[64:67]
	v_mfma_f32_16x16x32_f16 v[64:67], v[182:185], v[150:153], v[64:67]
	v_mfma_f32_16x16x32_f16 v[68:71], v[186:189], v[146:149], v[68:71]
	v_mfma_f32_16x16x32_f16 v[68:71], v[190:193], v[150:153], v[68:71]
	v_mfma_f32_16x16x32_f16 v[72:75], v[178:181], v[154:157], v[72:75]
	v_mfma_f32_16x16x32_f16 v[72:75], v[182:185], v[158:161], v[72:75]
	v_mfma_f32_16x16x32_f16 v[76:79], v[186:189], v[154:157], v[76:79]
	v_mfma_f32_16x16x32_f16 v[76:79], v[190:193], v[158:161], v[76:79]
	v_mfma_f32_16x16x32_f16 v[80:83], v[178:181], v[162:165], v[80:83]
	v_mfma_f32_16x16x32_f16 v[80:83], v[182:185], v[166:169], v[80:83]
	v_mfma_f32_16x16x32_f16 v[84:87], v[186:189], v[162:165], v[84:87]
	v_mfma_f32_16x16x32_f16 v[84:87], v[190:193], v[166:169], v[84:87]
	v_mfma_f32_16x16x32_f16 v[88:91], v[178:181], v[170:173], v[88:91]
	v_mfma_f32_16x16x32_f16 v[88:91], v[182:185], v[174:177], v[88:91]
	v_mfma_f32_16x16x32_f16 v[92:95], v[186:189], v[170:173], v[92:95]
	v_mfma_f32_16x16x32_f16 v[92:95], v[190:193], v[174:177], v[92:95]
	s_setprio 0
	s_addk_i32 s7, 0x100
	s_cmp_lt_u32 s8, 32
	s_mov_b32 s8, s9
	s_barrier
	s_cbranch_scc1 .LBB1_82
	ds_read_b128 v[132:135], v219 offset:32768
	ds_read_b128 v[136:139], v219 offset:33792
	ds_read_b128 v[140:143], v219 offset:34816
	ds_read_b128 v[144:147], v219 offset:35840
	ds_read_b128 v[128:131], v220
	ds_read_b128 v[148:151], v220 offset:1024
	ds_read_b128 v[152:155], v221
	ds_read_b128 v[156:159], v221 offset:1024
	ds_read_b128 v[188:191], v222
	ds_read_b128 v[192:195], v222 offset:1024
	ds_read_b128 v[196:199], v223
	ds_read_b128 v[200:203], v223 offset:1024
	s_setprio 2
	s_lshl_b32 s3, s50, 9
	s_add_i32 s3, s47, s3
	s_add_i32 s3, s3, 0x10380
	s_mov_b32 m0, s43
	v_add_u32_e32 v160, s3, v206
	global_load_lds_dwordx4 v160, s[18:19]
	v_add_u32_e32 v160, s3, v213
	s_mov_b32 m0, s44
	s_nop 0
	global_load_lds_dwordx4 v160, s[18:19]
	s_setprio 0
	s_waitcnt vmcnt(8)
	s_waitcnt lgkmcnt(0)
	s_barrier
	s_waitcnt lgkmcnt(0)
	s_setprio 1
	s_waitcnt lgkmcnt(0)
	v_mfma_f32_16x16x32_f16 v[124:127], v[132:135], v[128:131], v[124:127]
	v_mfma_f32_16x16x32_f16 v[120:123], v[140:143], v[128:131], v[120:123]
	v_mfma_f32_16x16x32_f16 v[116:119], v[132:135], v[152:155], v[116:119]
	v_mfma_f32_16x16x32_f16 v[112:115], v[140:143], v[152:155], v[112:115]
	v_mfma_f32_16x16x32_f16 v[108:111], v[132:135], v[188:191], v[108:111]
	v_mfma_f32_16x16x32_f16 v[104:107], v[140:143], v[188:191], v[104:107]
	v_mfma_f32_16x16x32_f16 v[100:103], v[132:135], v[196:199], v[100:103]
	v_mfma_f32_16x16x32_f16 v[96:99], v[140:143], v[196:199], v[96:99]
	v_mfma_f32_16x16x32_f16 v[160:163], v[136:139], v[148:151], v[124:127]
	v_mfma_f32_16x16x32_f16 v[164:167], v[144:147], v[148:151], v[120:123]
	v_mfma_f32_16x16x32_f16 v[168:171], v[136:139], v[156:159], v[116:119]
	v_mfma_f32_16x16x32_f16 v[172:175], v[144:147], v[156:159], v[112:115]
	v_mfma_f32_16x16x32_f16 v[176:179], v[136:139], v[192:195], v[108:111]
	v_mfma_f32_16x16x32_f16 v[180:183], v[144:147], v[192:195], v[104:107]
	v_mfma_f32_16x16x32_f16 v[100:103], v[136:139], v[200:203], v[100:103]
	v_mfma_f32_16x16x32_f16 v[184:187], v[144:147], v[200:203], v[96:99]
	s_setprio 0
	s_barrier
	ds_read_b128 v[104:107], v219 offset:49152
	ds_read_b128 v[108:111], v219 offset:50176
	ds_read_b128 v[116:119], v219 offset:51200
	ds_read_b128 v[236:239], v219 offset:52224
	s_waitcnt lgkmcnt(0)
	s_barrier
	s_waitcnt lgkmcnt(0)
	s_setprio 1
	s_waitcnt lgkmcnt(0)
	v_mfma_f32_16x16x32_f16 v[52:55], v[104:107], v[128:131], v[52:55]
	v_mfma_f32_16x16x32_f16 v[40:43], v[116:119], v[128:131], v[40:43]
	v_mfma_f32_16x16x32_f16 v[36:39], v[104:107], v[152:155], v[36:39]
	v_mfma_f32_16x16x32_f16 v[32:35], v[116:119], v[152:155], v[32:35]
	v_mfma_f32_16x16x32_f16 v[28:31], v[104:107], v[188:191], v[28:31]
	v_mfma_f32_16x16x32_f16 v[24:27], v[116:119], v[188:191], v[24:27]
	v_mfma_f32_16x16x32_f16 v[20:23], v[104:107], v[196:199], v[20:23]
	v_mfma_f32_16x16x32_f16 v[16:19], v[116:119], v[196:199], v[16:19]
	v_mfma_f32_16x16x32_f16 v[52:55], v[108:111], v[148:151], v[52:55]
	v_mfma_f32_16x16x32_f16 v[40:43], v[236:239], v[148:151], v[40:43]
	v_mfma_f32_16x16x32_f16 v[36:39], v[108:111], v[156:159], v[36:39]
	v_mfma_f32_16x16x32_f16 v[32:35], v[236:239], v[156:159], v[32:35]
	v_mfma_f32_16x16x32_f16 v[28:31], v[108:111], v[192:195], v[28:31]
	v_mfma_f32_16x16x32_f16 v[24:27], v[236:239], v[192:195], v[24:27]
	v_mfma_f32_16x16x32_f16 v[96:99], v[108:111], v[200:203], v[20:23]
	v_mfma_f32_16x16x32_f16 v[16:19], v[236:239], v[200:203], v[16:19]
	s_setprio 0
	s_barrier
	ds_read_b128 v[20:23], v220 offset:16384
	ds_read_b128 v[148:151], v220 offset:17408
	ds_read_b128 v[152:155], v221 offset:16384
	ds_read_b128 v[156:159], v221 offset:17408
	ds_read_b128 v[188:191], v222 offset:16384
	ds_read_b128 v[192:195], v222 offset:17408
	ds_read_b128 v[196:199], v223 offset:16384
	ds_read_b128 v[200:203], v223 offset:17408
	s_waitcnt vmcnt(4)
	s_waitcnt lgkmcnt(0)
	s_barrier
	s_waitcnt lgkmcnt(0)
	s_setprio 1
	s_waitcnt lgkmcnt(0)
	v_mfma_f32_16x16x32_f16 v[0:3], v[140:143], v[152:155], v[0:3]
	v_mfma_f32_16x16x32_f16 v[124:127], v[144:147], v[156:159], v[0:3]
	v_mfma_f32_16x16x32_f16 v[0:3], v[132:135], v[188:191], v[44:47]
	v_mfma_f32_16x16x32_f16 v[128:131], v[136:139], v[192:195], v[0:3]
	v_mfma_f32_16x16x32_f16 v[0:3], v[140:143], v[188:191], v[48:51]
	v_mfma_f32_16x16x32_f16 v[48:51], v[144:147], v[192:195], v[0:3]
	v_mfma_f32_16x16x32_f16 v[0:3], v[132:135], v[196:199], v[56:59]
	v_mfma_f32_16x16x32_f16 v[12:15], v[132:135], v[20:23], v[12:15]
	v_mfma_f32_16x16x32_f16 v[8:11], v[140:143], v[20:23], v[8:11]
	v_mfma_f32_16x16x32_f16 v[4:7], v[132:135], v[152:155], v[4:7]
	v_mfma_f32_16x16x32_f16 v[56:59], v[136:139], v[200:203], v[0:3]
	v_mfma_f32_16x16x32_f16 v[0:3], v[140:143], v[196:199], v[60:63]
	v_mfma_f32_16x16x32_f16 v[112:115], v[136:139], v[148:151], v[12:15]
	v_mfma_f32_16x16x32_f16 v[8:11], v[144:147], v[148:151], v[8:11]
	v_mfma_f32_16x16x32_f16 v[120:123], v[136:139], v[156:159], v[4:7]
	v_mfma_f32_16x16x32_f16 v[60:63], v[144:147], v[200:203], v[0:3]
	s_setprio 0
	s_setprio 1
	v_mfma_f32_16x16x32_f16 v[0:3], v[104:107], v[20:23], v[64:67]
	v_mfma_f32_16x16x32_f16 v[132:135], v[108:111], v[148:151], v[0:3]
	v_mfma_f32_16x16x32_f16 v[0:3], v[116:119], v[20:23], v[68:71]
	v_mfma_f32_16x16x32_f16 v[136:139], v[236:239], v[148:151], v[0:3]
	v_mfma_f32_16x16x32_f16 v[0:3], v[104:107], v[152:155], v[72:75]
	v_mfma_f32_16x16x32_f16 v[140:143], v[108:111], v[156:159], v[0:3]
	v_mfma_f32_16x16x32_f16 v[0:3], v[116:119], v[152:155], v[76:79]
	v_mfma_f32_16x16x32_f16 v[144:147], v[236:239], v[156:159], v[0:3]
	v_mfma_f32_16x16x32_f16 v[0:3], v[104:107], v[188:191], v[80:83]
	v_mfma_f32_16x16x32_f16 v[80:83], v[108:111], v[192:195], v[0:3]
	v_mfma_f32_16x16x32_f16 v[0:3], v[116:119], v[188:191], v[84:87]
	v_mfma_f32_16x16x32_f16 v[148:151], v[236:239], v[192:195], v[0:3]
	v_mfma_f32_16x16x32_f16 v[0:3], v[104:107], v[196:199], v[88:91]
	v_mfma_f32_16x16x32_f16 v[152:155], v[108:111], v[200:203], v[0:3]
	v_mfma_f32_16x16x32_f16 v[0:3], v[116:119], v[196:199], v[92:95]
	v_mfma_f32_16x16x32_f16 v[156:159], v[236:239], v[200:203], v[0:3]
	s_setprio 0
	s_add_i32 s49, s49, s17
	s_cmpk_lt_i32 s49, 0x1c8
	s_cselect_b64 s[6:7], -1, 0
	s_cmpk_gt_i32 s49, 0x1c7
	s_cselect_b64 s[12:13], -1, 0
	s_and_b64 vcc, exec, s[12:13]
	s_mov_b32 s54, s2
	s_mov_b32 s53, s51
	s_mov_b32 s55, s52
	s_barrier
	s_cbranch_vccnz .LBB1_100
	s_cmpk_lt_i32 s49, 0x148
	s_cbranch_scc1 .LBB1_88
	s_cmpk_lt_u32 s49, 0x1a0
	s_cbranch_scc1 .LBB1_89
	s_cmpk_lt_u32 s49, 0x1b8
	s_cbranch_scc1 .LBB1_90
	s_cmpk_lt_u32 s49, 0x1c0
	s_cselect_b32 s47, s45, 0xfffffe40
	s_cselect_b32 s48, 3, 4
	s_mov_b32 s3, 1
	s_cmp_lt_i32 s48, 1
	s_movk_i32 s53, 0x64
	s_cbranch_scc0 .LBB1_91
	s_branch .LBB1_99
